# diff-attention: zero-start score accumulators via MFMA C=0 (no 32x v_mov per sub-head) + K-read pipelining + 128-cycle spacer after sub-head-0 softmax
# baseline (speedup 1.0000x reference)
.Lz_l1s0:
	v_add_u32_e32 v0, s49, v225
	v_add_u32_e32 v6, v0, v227
	v_add_u32_e32 v7, v0, v228
	ds_read_b128 v[244:247], v6
	ds_read_b128 v[248:251], v6 offset:8192
	ds_read_b128 v[236:239], v7
	ds_read_b128 v[208:211], v7 offset:8192
	v_add_u32_e32 v6, v0, v229
	v_add_u32_e32 v7, v0, v230
	ds_read_b128 v[2:5], v6
	ds_read_b128 v[8:11], v6 offset:8192
	ds_read_b128 v[12:15], v7
	s_xor_b64 s[44:45], s[44:45], -1
	v_add_u32_e32 v6, v0, v226
	s_waitcnt lgkmcnt(6)
	v_mfma_f32_32x32x16_bf16 v[144:159], v[244:247], v[176:179], 0
	ds_read_b128 v[244:247], v7 offset:8192
	s_waitcnt lgkmcnt(6)
	v_mfma_f32_32x32x16_bf16 v[160:175], v[248:251], v[176:179], 0
	s_branch .Lc_l1s0
.Lz_l1s1:
	v_add_u32_e32 v212, v0, v231
	v_add_u32_e32 v213, v0, v232
	v_add_u32_e32 v0, v0, v233
	s_waitcnt lgkmcnt(0)
	v_mfma_f32_32x32x16_bf16 v[160:175], v[248:251], v[192:195], 0
	ds_read_b128 v[248:251], v212 offset:8192
	v_mfma_f32_32x32x16_bf16 v[144:159], v[236:239], v[192:195], 0
	s_branch .Lc_l1s1

.LBB0_194:
	s_and_b64 vcc, exec, s[44:45]
	s_cbranch_vccnz .Lz_l1s0
	v_mov_b32_e32 v144, v223
	v_mov_b32_e32 v145, v223
	v_mov_b32_e32 v146, v223
	v_mov_b32_e32 v147, v223
	v_mov_b32_e32 v148, v223
	v_mov_b32_e32 v149, v223
	v_mov_b32_e32 v150, v223
	v_mov_b32_e32 v151, v223
	v_mov_b32_e32 v152, v223
	v_mov_b32_e32 v153, v223
	v_mov_b32_e32 v154, v223
	v_mov_b32_e32 v155, v223
	v_mov_b32_e32 v156, v223
	v_mov_b32_e32 v157, v223
	v_mov_b32_e32 v158, v223
	v_mov_b32_e32 v159, v223
	v_mov_b32_e32 v160, v223
	v_mov_b32_e32 v161, v223
	v_mov_b32_e32 v162, v223
	v_mov_b32_e32 v163, v223
	v_mov_b32_e32 v164, v223
	v_mov_b32_e32 v165, v223
	v_mov_b32_e32 v166, v223
	v_mov_b32_e32 v167, v223
	v_mov_b32_e32 v168, v223
	v_mov_b32_e32 v169, v223
	v_mov_b32_e32 v170, v223
	v_mov_b32_e32 v171, v223
	v_mov_b32_e32 v172, v223
	v_mov_b32_e32 v173, v223
	v_mov_b32_e32 v174, v223
	v_mov_b32_e32 v175, v223

.Lc_l1s0:
	s_waitcnt lgkmcnt(5)
	v_mfma_f32_32x32x16_bf16 v[144:159], v[236:239], v[180:183], v[144:159]
	ds_read_b128 v[248:251], v6
	ds_read_b128 v[236:239], v6 offset:8192
	s_waitcnt lgkmcnt(6)
	v_mfma_f32_32x32x16_bf16 v[160:175], v[208:211], v[180:183], v[160:175]
	v_add_u32_e32 v7, v0, v231
	s_waitcnt lgkmcnt(5)
	v_mfma_f32_32x32x16_bf16 v[144:159], v[2:5], v[184:187], v[144:159]
	s_waitcnt lgkmcnt(4)
	v_mfma_f32_32x32x16_bf16 v[160:175], v[8:11], v[184:187], v[160:175]
	s_waitcnt lgkmcnt(3)
	v_mfma_f32_32x32x16_bf16 v[144:159], v[12:15], v[188:191], v[144:159]
	s_waitcnt lgkmcnt(2)
	v_mfma_f32_32x32x16_bf16 v[160:175], v[244:247], v[188:191], v[160:175]
	ds_read_b128 v[244:247], v7
	s_nop 9
	v_exp_f32_e32 v6, v144
	v_exp_f32_e32 v3, v145
	v_exp_f32_e32 v10, v148
	v_exp_f32_e32 v11, v149
	v_exp_f32_e32 v12, v150
	v_exp_f32_e32 v148, v152
	v_exp_f32_e32 v150, v153
	v_exp_f32_e32 v156, v156
	v_exp_f32_e32 v157, v157
	v_exp_f32_e32 v5, v146
	v_exp_f32_e32 v152, v154
	v_exp_f32_e32 v158, v158
	v_exp_f32_e32 v8, v147
	v_exp_f32_e32 v13, v151
	v_exp_f32_e32 v154, v155
	v_exp_f32_e32 v159, v159
	v_exp_f32_e32 v2, v160
	v_exp_f32_e32 v144, v164
	v_exp_f32_e32 v149, v168
	v_exp_f32_e32 v160, v172
	v_exp_f32_e32 v4, v161
	v_exp_f32_e32 v145, v165
	v_exp_f32_e32 v151, v169
	v_exp_f32_e32 v161, v173
	v_add_f32_e32 v14, v6, v3
	v_add_f32_e32 v15, v10, v11
	v_add_f32_e32 v164, v148, v150
	v_add_f32_e32 v165, v156, v157
	v_exp_f32_e32 v7, v162
	v_exp_f32_e32 v146, v166
	v_exp_f32_e32 v153, v170
	v_exp_f32_e32 v162, v174
	v_add_f32_e32 v14, v5, v14
	v_add_f32_e32 v15, v12, v15
	v_add_f32_e32 v164, v152, v164
	v_add_f32_e32 v165, v158, v165
	v_exp_f32_e32 v9, v163
	v_exp_f32_e32 v147, v167
	v_exp_f32_e32 v155, v171
	v_exp_f32_e32 v163, v175
	v_add_f32_e32 v14, v8, v14
	v_add_f32_e32 v15, v13, v15
	v_add_f32_e32 v164, v154, v164
	v_add_f32_e32 v165, v159, v165
	v_add_f32_e32 v14, v2, v14
	v_add_f32_e32 v15, v144, v15
	v_add_f32_e32 v164, v149, v164
	v_add_f32_e32 v165, v160, v165
	v_add_f32_e32 v14, v4, v14
	v_add_f32_e32 v15, v145, v15
	v_add_f32_e32 v164, v151, v164
	v_add_f32_e32 v165, v161, v165
	v_add_f32_e32 v14, v7, v14
	v_add_f32_e32 v15, v146, v15
	v_add_f32_e32 v164, v153, v164
	v_add_f32_e32 v165, v162, v165
	v_add_f32_e32 v14, v9, v14
	v_add_f32_e32 v15, v147, v15
	v_add_f32_e32 v164, v155, v164
	v_add_f32_e32 v165, v163, v165
	v_add_f32_e32 v14, v14, v15
	v_add_f32_e32 v15, v164, v165
	v_add_f32_e32 v14, v14, v15
	v_mov_b32_e32 v15, v14
	v_cvt_pk_bf16_f32 v208, v6, v3
	v_cvt_pk_bf16_f32 v209, v5, v8
	v_cvt_pk_bf16_f32 v210, v10, v11
	v_cvt_pk_bf16_f32 v211, v12, v13
	v_cvt_pk_bf16_f32 v10, v148, v150
	v_cvt_pk_bf16_f32 v11, v152, v154
	v_cvt_pk_bf16_f32 v12, v156, v157
	v_cvt_pk_bf16_f32 v13, v158, v159
	v_cvt_pk_bf16_f32 v6, v2, v4
	v_cvt_pk_bf16_f32 v7, v7, v9
	v_cvt_pk_bf16_f32 v8, v144, v145
	v_cvt_pk_bf16_f32 v9, v146, v147
	v_cvt_pk_bf16_f32 v2, v149, v151
	v_cvt_pk_bf16_f32 v3, v153, v155
	v_cvt_pk_bf16_f32 v4, v160, v161
	v_cvt_pk_bf16_f32 v5, v162, v163
	v_permlane32_swap_b32_e32 v14, v15
	v_permlane32_swap_b32_e32 v208, v210
	v_permlane32_swap_b32_e32 v209, v211
	v_permlane32_swap_b32_e32 v10, v12
	v_permlane32_swap_b32_e32 v11, v13
	v_permlane32_swap_b32_e32 v6, v8
	v_permlane32_swap_b32_e32 v7, v9
	v_permlane32_swap_b32_e32 v2, v4
	v_permlane32_swap_b32_e32 v3, v5
	s_nop 15
	s_nop 15
	s_andn2_b64 vcc, exec, s[44:45]
	s_cbranch_vccnz .Lz_l1s1
	s_andn2_b64 vcc, exec, s[42:43]
	s_mov_b64 s[42:43], -1
	s_cbranch_vccnz .LBB0_198
	v_add_u32_e32 v144, 0x21780, v212
	v_add_u32_e32 v146, 0x21708, v212
	v_add_u32_e32 v147, 0x21788, v212
	v_add_u32_e32 v148, 0x21720, v212
	v_add_u32_e32 v149, 0x217a0, v212
	v_add_u32_e32 v150, 0x21728, v212
	v_add_u32_e32 v151, 0x217a8, v212
	v_add_u32_e32 v152, 0x21740, v212
	v_add_u32_e32 v153, 0x217c0, v212
	v_add_u32_e32 v154, 0x21748, v212
	v_add_u32_e32 v155, 0x217c8, v212
	v_add_u32_e32 v156, 0x21760, v212
	v_add_u32_e32 v157, 0x217e0, v212
	v_add_u32_e32 v158, 0x21768, v212
	v_add_u32_e32 v159, 0x217e8, v212
	ds_read2_b32 v[160:161], v213 offset1:1
	ds_read2_b32 v[144:145], v144 offset1:1
	ds_read2_b32 v[162:163], v146 offset1:1
	ds_read2_b32 v[146:147], v147 offset1:1
	ds_read2_b32 v[164:165], v148 offset1:1
	ds_read2_b32 v[148:149], v149 offset1:1
	ds_read2_b32 v[166:167], v150 offset1:1
	ds_read2_b32 v[150:151], v151 offset1:1
	ds_read2_b32 v[168:169], v152 offset1:1
	ds_read2_b32 v[152:153], v153 offset1:1
	ds_read2_b32 v[170:171], v154 offset1:1
	ds_read2_b32 v[154:155], v155 offset1:1
	ds_read2_b32 v[172:173], v156 offset1:1
	ds_read2_b32 v[156:157], v157 offset1:1
	ds_read2_b32 v[174:175], v158 offset1:1
	ds_read2_b32 v[158:159], v159 offset1:1
	s_mov_b64 s[42:43], 0

.Lc_l1s1:
	ds_read_b128 v[236:239], v213
	v_mfma_f32_32x32x16_bf16 v[160:175], v[244:247], v[196:199], v[160:175]
	ds_read_b128 v[244:247], v213 offset:8192
	s_waitcnt lgkmcnt(2)
	v_mfma_f32_32x32x16_bf16 v[144:159], v[248:251], v[196:199], v[144:159]
	ds_read_b128 v[248:251], v0
	s_waitcnt lgkmcnt(2)
	v_mfma_f32_32x32x16_bf16 v[160:175], v[236:239], v[200:203], v[160:175]
	ds_read_b128 v[236:239], v0 offset:8192
	s_waitcnt lgkmcnt(2)
	v_mfma_f32_32x32x16_bf16 v[144:159], v[244:247], v[200:203], v[144:159]
	v_add_f32_e32 v0, v14, v15
	v_add_f32_e32 v235, v235, v0
	s_waitcnt lgkmcnt(1)
	v_mfma_f32_32x32x16_bf16 v[160:175], v[248:251], v[204:207], v[160:175]
	s_waitcnt lgkmcnt(0)
	v_mfma_f32_32x32x16_bf16 v[144:159], v[236:239], v[204:207], v[144:159]
	s_nop 10
	v_exp_f32_e32 v14, v160
	v_exp_f32_e32 v160, v161
	v_exp_f32_e32 v164, v164
	v_exp_f32_e32 v15, v168
	v_exp_f32_e32 v161, v169
	v_exp_f32_e32 v162, v162
	v_exp_f32_e32 v220, v163
	v_exp_f32_e32 v166, v166
	s_nop 4
	v_exp_f32_e32 v246, v148
	v_exp_f32_e32 v148, v165
	v_exp_f32_e32 v248, v149
	v_exp_f32_e32 v165, v172
	v_exp_f32_e32 v149, v173
	v_exp_f32_e32 v250, v150
	v_exp_f32_e32 v150, v167
	v_exp_f32_e32 v163, v170
	v_exp_f32_e32 v167, v174
	v_exp_f32_e32 v252, v151
	v_exp_f32_e32 v221, v171
	v_exp_f32_e32 v151, v175
	v_exp_f32_e32 v144, v144
	v_exp_f32_e32 v212, v145
	v_exp_f32_e32 v145, v152
	v_exp_f32_e32 v247, v156
	v_exp_f32_e32 v244, v147
	v_exp_f32_e32 v213, v153
	v_exp_f32_e32 v147, v154
	v_exp_f32_e32 v245, v155
	v_exp_f32_e32 v249, v157
	v_pk_add_f32 v[152:153], v[14:15], v[160:161]
	v_pk_add_f32 v[154:155], v[164:165], v[148:149]
	v_exp_f32_e32 v146, v146
	v_exp_f32_e32 v251, v158
	v_pk_add_f32 v[152:153], v[162:163], v[152:153]
	v_pk_add_f32 v[154:155], v[166:167], v[154:155]
	v_exp_f32_e32 v253, v159
	v_pk_add_f32 v[152:153], v[220:221], v[152:153]
	v_pk_add_f32 v[154:155], v[150:151], v[154:155]
	v_pk_add_f32 v[152:153], v[144:145], v[152:153]
	v_pk_add_f32 v[154:155], v[246:247], v[154:155]
	v_pk_add_f32 v[152:153], v[212:213], v[152:153]
	v_pk_add_f32 v[154:155], v[248:249], v[154:155]
	v_pk_add_f32 v[152:153], v[146:147], v[152:153]
	v_pk_add_f32 v[154:155], v[250:251], v[154:155]
	v_pk_add_f32 v[152:153], v[244:245], v[152:153]
	v_pk_add_f32 v[154:155], v[252:253], v[154:155]
	v_cvt_pk_bf16_f32 v156, v14, v160
	v_pk_add_f32 v[152:153], v[152:153], v[154:155]
	v_cvt_pk_bf16_f32 v157, v162, v220
	v_pk_add_f32 v[152:153], v[152:153], v[152:153] op_sel:[0,1] op_sel_hi:[1,0]
	v_cvt_pk_bf16_f32 v158, v164, v148
	v_mov_b32_e32 v0, v152
	s_nop 1
	v_permlane32_swap_b32_e32 v152, v0
	v_add_f32_e32 v0, v152, v0
	v_cvt_pk_bf16_f32 v159, v166, v150
	v_cvt_pk_bf16_f32 v152, v15, v161
	v_cvt_pk_bf16_f32 v153, v163, v221
	v_cvt_pk_bf16_f32 v154, v165, v149
	v_cvt_pk_bf16_f32 v155, v167, v151
	v_cvt_pk_bf16_f32 v148, v144, v212
	v_cvt_pk_bf16_f32 v149, v146, v244
	v_cvt_pk_bf16_f32 v150, v246, v248
	v_cvt_pk_bf16_f32 v151, v250, v252
	v_cvt_pk_bf16_f32 v144, v145, v213
	v_cvt_pk_bf16_f32 v145, v147, v245
	v_cvt_pk_bf16_f32 v146, v247, v249
	v_cvt_pk_bf16_f32 v147, v251, v253
	v_add_f32_e32 v234, v234, v0
	v_permlane32_swap_b32_e32 v156, v158
	v_permlane32_swap_b32_e32 v157, v159
	v_permlane32_swap_b32_e32 v152, v154
	v_permlane32_swap_b32_e32 v153, v155
	v_permlane32_swap_b32_e32 v148, v150
	v_permlane32_swap_b32_e32 v149, v151
	v_permlane32_swap_b32_e32 v144, v146
	v_permlane32_swap_b32_e32 v145, v147
	s_add_i32 s42, s49, 0x4000
	s_cmpk_lg_u32 s49, 0xc000
	s_cselect_b32 s42, s42, 0
	s_add_i32 s43, s90, 0x4000
	s_cmpk_lg_u32 s90, 0xc000
	s_cselect_b32 s90, s43, 0
	s_add_u32 s40, s40, 0x60000
	s_addc_u32 s41, s41, 0
	s_addk_i32 s71, 0x100
	s_add_i32 s73, s73, 64
	s_add_i32 s86, s86, 1
	s_cmpk_eq_i32 s71, 0x4000
	s_cbranch_scc1 .LBB0_202
	s_mov_b32 s44, s49
	s_mov_b32 s49, s42
	s_cmpk_eq_i32 s71, 0x3f00
	s_mov_b64 s[42:43], -1
	s_cbranch_scc0 .LBB0_191
	s_branch .LBB0_185

.Lc_l2s1:
	ds_read_b128 v[236:239], v219 offset:8192
	v_mfma_f32_32x32x16_bf16 v[144:159], v[240:243], v[196:199], v[144:159]
	ds_read_b128 v[240:243], v212
	v_mfma_f32_32x32x16_bf16 v[160:175], v[244:247], v[196:199], v[160:175]
	ds_read_b128 v[244:247], v212 offset:8192
	s_waitcnt lgkmcnt(3)
	v_mfma_f32_32x32x16_bf16 v[144:159], v[248:251], v[200:203], v[144:159]
	s_waitcnt lgkmcnt(2)
	v_mfma_f32_32x32x16_bf16 v[160:175], v[236:239], v[200:203], v[160:175]
	v_add_f32_e32 v212, v213, v218
	v_add_f32_e32 v235, v235, v212
	s_waitcnt lgkmcnt(1)
	v_mfma_f32_32x32x16_bf16 v[144:159], v[240:243], v[204:207], v[144:159]
	s_waitcnt lgkmcnt(0)
	v_mfma_f32_32x32x16_bf16 v[160:175], v[244:247], v[204:207], v[160:175]
	s_nop 10
	v_exp_f32_e32 v212, v144
	v_exp_f32_e32 v218, v145
	v_exp_f32_e32 v242, v148
	v_exp_f32_e32 v244, v149
	v_exp_f32_e32 v213, v152
	v_exp_f32_e32 v219, v153
	v_exp_f32_e32 v243, v156
	v_exp_f32_e32 v245, v157
	v_exp_f32_e32 v236, v146
	v_exp_f32_e32 v150, v150
	v_exp_f32_e32 v248, v151
	v_exp_f32_e32 v237, v154
	v_exp_f32_e32 v151, v158
	v_exp_f32_e32 v238, v147
	v_exp_f32_e32 v239, v155
	v_exp_f32_e32 v249, v159
	v_exp_f32_e32 v160, v160
	v_exp_f32_e32 v220, v161
	v_exp_f32_e32 v164, v164
	v_exp_f32_e32 v246, v165
	v_exp_f32_e32 v161, v168
	v_exp_f32_e32 v165, v172
	v_exp_f32_e32 v221, v169
	v_exp_f32_e32 v247, v173
	v_pk_add_f32 v[144:145], v[212:213], v[218:219]
	v_pk_add_f32 v[146:147], v[242:243], v[244:245]
	v_exp_f32_e32 v162, v162
	v_exp_f32_e32 v240, v163
	v_exp_f32_e32 v166, v166
	v_exp_f32_e32 v250, v167
	v_exp_f32_e32 v163, v170
	v_exp_f32_e32 v167, v174
	v_pk_add_f32 v[144:145], v[236:237], v[144:145]
	v_pk_add_f32 v[146:147], v[150:151], v[146:147]
	v_exp_f32_e32 v241, v171
	v_exp_f32_e32 v251, v175
	v_pk_add_f32 v[144:145], v[238:239], v[144:145]
	v_pk_add_f32 v[146:147], v[248:249], v[146:147]
	v_pk_add_f32 v[144:145], v[160:161], v[144:145]
	v_pk_add_f32 v[146:147], v[164:165], v[146:147]
	v_pk_add_f32 v[144:145], v[220:221], v[144:145]
	v_pk_add_f32 v[146:147], v[246:247], v[146:147]
	v_pk_add_f32 v[144:145], v[162:163], v[144:145]
	v_pk_add_f32 v[146:147], v[166:167], v[146:147]
	v_pk_add_f32 v[144:145], v[240:241], v[144:145]
	v_pk_add_f32 v[146:147], v[250:251], v[146:147]
	v_cvt_pk_bf16_f32 v148, v213, v219
	v_pk_add_f32 v[144:145], v[144:145], v[146:147]
	v_cvt_pk_bf16_f32 v146, v242, v244
	v_pk_add_f32 v[144:145], v[144:145], v[144:145] op_sel:[0,1] op_sel_hi:[1,0]
	v_cvt_pk_bf16_f32 v147, v150, v248
	v_mov_b32_e32 v145, v144
	s_nop 1
	v_permlane32_swap_b32_e32 v144, v145
	v_add_f32_e32 v144, v144, v145
	v_add_f32_e32 v234, v234, v144
	v_cvt_pk_bf16_f32 v144, v212, v218
	v_cvt_pk_bf16_f32 v145, v236, v238
	v_cvt_pk_bf16_f32 v149, v237, v239
	v_cvt_pk_bf16_f32 v150, v243, v245
	v_cvt_pk_bf16_f32 v151, v151, v249
	v_cvt_pk_bf16_f32 v152, v160, v220
	v_cvt_pk_bf16_f32 v153, v162, v240
	v_cvt_pk_bf16_f32 v154, v164, v246
	v_cvt_pk_bf16_f32 v155, v166, v250
	v_cvt_pk_bf16_f32 v156, v161, v221
	v_cvt_pk_bf16_f32 v157, v163, v241
	v_cvt_pk_bf16_f32 v158, v165, v247
	v_cvt_pk_bf16_f32 v159, v167, v251
	v_permlane32_swap_b32_e32 v144, v146
	v_permlane32_swap_b32_e32 v145, v147
	v_permlane32_swap_b32_e32 v148, v150
	v_permlane32_swap_b32_e32 v149, v151
	v_permlane32_swap_b32_e32 v152, v154
	v_permlane32_swap_b32_e32 v153, v155
	v_permlane32_swap_b32_e32 v156, v158
	v_permlane32_swap_b32_e32 v157, v159
	s_waitcnt lgkmcnt(0)
	v_add_u32_e32 v212, s56, v224
	ds_read_b64_tr_b16 v[160:161], v212 offset:0
	ds_read_b64_tr_b16 v[162:163], v212 offset:0x800
	ds_read_b64_tr_b16 v[164:165], v212 offset:0x200
	ds_read_b64_tr_b16 v[166:167], v212 offset:0xa00
	ds_read_b64_tr_b16 v[168:169], v212 offset:0x400
	ds_read_b64_tr_b16 v[170:171], v212 offset:0xc00
	ds_read_b64_tr_b16 v[172:173], v212 offset:0x600
	ds_read_b64_tr_b16 v[174:175], v212 offset:0xe00
	s_waitcnt lgkmcnt(4)
	s_nop 0
	v_mfma_f32_32x32x16_bf16 v[112:127], v[208:211], v[160:163], v[112:127]
	v_mfma_f32_32x32x16_bf16 v[96:111], v[208:211], v[164:167], v[96:111]
	v_mfma_f32_32x32x16_bf16 v[128:143], v[144:147], v[160:163], v[128:143]
	v_mfma_f32_32x32x16_bf16 v[80:95], v[144:147], v[164:167], v[80:95]
	ds_read_b64_tr_b16 v[160:161], v212 offset:0x1000
	ds_read_b64_tr_b16 v[162:163], v212 offset:0x1800
	ds_read_b64_tr_b16 v[164:165], v212 offset:0x1200
	ds_read_b64_tr_b16 v[166:167], v212 offset:0x1a00
	s_waitcnt lgkmcnt(4)
	v_mfma_f32_32x32x16_bf16 v[64:79], v[208:211], v[168:171], v[64:79]
	v_mfma_f32_32x32x16_bf16 v[48:63], v[208:211], v[172:175], v[48:63]
	v_mfma_f32_32x32x16_bf16 v[32:47], v[144:147], v[168:171], v[32:47]
	v_mfma_f32_32x32x16_bf16 v[16:31], v[144:147], v[172:175], v[16:31]
	ds_read_b64_tr_b16 v[144:145], v212 offset:0x1400
	ds_read_b64_tr_b16 v[146:147], v212 offset:0x1c00
	ds_read_b64_tr_b16 v[168:169], v212 offset:0x1600
	ds_read_b64_tr_b16 v[170:171], v212 offset:0x1e00
	s_waitcnt lgkmcnt(4)
	v_mfma_f32_32x32x16_bf16 v[112:127], v[10:13], v[160:163], v[112:127]
	v_mfma_f32_32x32x16_bf16 v[96:111], v[10:13], v[164:167], v[96:111]
	v_mfma_f32_32x32x16_bf16 v[128:143], v[148:151], v[160:163], v[128:143]
	v_mfma_f32_32x32x16_bf16 v[80:95], v[148:151], v[164:167], v[80:95]
	ds_read_b64_tr_b16 v[160:161], v212 offset:0x2000
	ds_read_b64_tr_b16 v[162:163], v212 offset:0x2800
	ds_read_b64_tr_b16 v[164:165], v212 offset:0x2200
	ds_read_b64_tr_b16 v[166:167], v212 offset:0x2a00
	s_waitcnt lgkmcnt(4)
	v_mfma_f32_32x32x16_bf16 v[64:79], v[10:13], v[144:147], v[64:79]
	v_mfma_f32_32x32x16_bf16 v[48:63], v[10:13], v[168:171], v[48:63]
	v_mfma_f32_32x32x16_bf16 v[32:47], v[148:151], v[144:147], v[32:47]
	v_mfma_f32_32x32x16_bf16 v[16:31], v[148:151], v[168:171], v[16:31]
	ds_read_b64_tr_b16 v[10:11], v212 offset:0x2400
	ds_read_b64_tr_b16 v[12:13], v212 offset:0x2c00
	ds_read_b64_tr_b16 v[144:145], v212 offset:0x2600
	ds_read_b64_tr_b16 v[146:147], v212 offset:0x2e00
	s_waitcnt lgkmcnt(4)
	v_mfma_f32_32x32x16_bf16 v[112:127], v[6:9], v[160:163], v[112:127]
	v_mfma_f32_32x32x16_bf16 v[96:111], v[6:9], v[164:167], v[96:111]
	v_mfma_f32_32x32x16_bf16 v[128:143], v[152:155], v[160:163], v[128:143]
	v_mfma_f32_32x32x16_bf16 v[80:95], v[152:155], v[164:167], v[80:95]
	ds_read_b64_tr_b16 v[148:149], v212 offset:0x3000
	ds_read_b64_tr_b16 v[150:151], v212 offset:0x3800
	ds_read_b64_tr_b16 v[160:161], v212 offset:0x3200
	ds_read_b64_tr_b16 v[162:163], v212 offset:0x3a00
	s_waitcnt lgkmcnt(4)
	v_mfma_f32_32x32x16_bf16 v[64:79], v[6:9], v[10:13], v[64:79]
	v_mfma_f32_32x32x16_bf16 v[48:63], v[6:9], v[144:147], v[48:63]
	v_mfma_f32_32x32x16_bf16 v[32:47], v[152:155], v[10:13], v[32:47]
	v_mfma_f32_32x32x16_bf16 v[16:31], v[152:155], v[144:147], v[16:31]
	ds_read_b64_tr_b16 v[6:7], v212 offset:0x3400
	ds_read_b64_tr_b16 v[8:9], v212 offset:0x3c00
	ds_read_b64_tr_b16 v[10:11], v212 offset:0x3600
	ds_read_b64_tr_b16 v[12:13], v212 offset:0x3e00
	s_waitcnt lgkmcnt(4)
	v_mfma_f32_32x32x16_bf16 v[112:127], v[2:5], v[148:151], v[112:127]
	v_mfma_f32_32x32x16_bf16 v[96:111], v[2:5], v[160:163], v[96:111]
	v_mfma_f32_32x32x16_bf16 v[128:143], v[156:159], v[148:151], v[128:143]
	v_mfma_f32_32x32x16_bf16 v[80:95], v[156:159], v[160:163], v[80:95]
	s_waitcnt lgkmcnt(0)
	v_mfma_f32_32x32x16_bf16 v[64:79], v[2:5], v[6:9], v[64:79]
	v_mfma_f32_32x32x16_bf16 v[48:63], v[2:5], v[10:13], v[48:63]
	v_mfma_f32_32x32x16_bf16 v[32:47], v[156:159], v[6:9], v[32:47]
	v_mfma_f32_32x32x16_bf16 v[16:31], v[156:159], v[10:13], v[16:31]
	s_add_i32 s42, s56, 0x4000
	s_cmpk_lg_u32 s56, 0xc000
	s_cselect_b32 s56, s42, 0
	s_add_i32 s42, s90, 0x4000
	s_cmpk_lg_u32 s90, 0xc000
	s_cselect_b32 s90, s42, 0
	s_add_u32 s40, s40, 0x60000
	s_addc_u32 s41, s41, 0
	s_addk_i32 s73, 0x100
	s_add_i32 s72, s72, 64
	s_add_i32 s71, s71, 1
	s_cmpk_eq_i32 s73, 0x4000
	s_cbranch_scc1 .LBB0_220

.Lz_l2s0:
	v_add_u32_e32 v212, s56, v225
	v_add_u32_e32 v6, v212, v227
	v_add_u32_e32 v7, v212, v228
	ds_read_b128 v[244:247], v6
	ds_read_b128 v[248:251], v6 offset:8192
	ds_read_b128 v[236:239], v7
	ds_read_b128 v[240:243], v7 offset:8192
	v_add_u32_e32 v6, v212, v229
	v_add_u32_e32 v7, v212, v230
	ds_read_b128 v[2:5], v6
	ds_read_b128 v[8:11], v6 offset:8192
	ds_read_b128 v[208:211], v7
	s_xor_b64 s[44:45], s[44:45], -1
	v_add_u32_e32 v6, v212, v226
	s_waitcnt lgkmcnt(6)
	v_mfma_f32_32x32x16_bf16 v[160:175], v[244:247], v[176:179], 0
	ds_read_b128 v[244:247], v7 offset:8192
	s_waitcnt lgkmcnt(6)
	v_mfma_f32_32x32x16_bf16 v[144:159], v[248:251], v[176:179], 0
	s_branch .Lc_l2s0
.Lz_l2s1:
	v_add_u32_e32 v219, v212, v232
	v_add_u32_e32 v212, v212, v233
	s_waitcnt lgkmcnt(0)
	v_mfma_f32_32x32x16_bf16 v[144:159], v[248:251], v[192:195], 0
	ds_read_b128 v[248:251], v219
	v_mfma_f32_32x32x16_bf16 v[160:175], v[236:239], v[192:195], 0
	s_branch .Lc_l2s1

.Lc_l2s0:
	s_waitcnt lgkmcnt(5)
	v_mfma_f32_32x32x16_bf16 v[160:175], v[236:239], v[180:183], v[160:175]
	v_add_u32_e32 v7, v212, v231
	s_waitcnt lgkmcnt(4)
	v_mfma_f32_32x32x16_bf16 v[144:159], v[240:243], v[180:183], v[144:159]
	ds_read_b128 v[248:251], v6
	ds_read_b128 v[236:239], v6 offset:8192
	ds_read_b128 v[240:243], v7
	s_waitcnt lgkmcnt(6)
	v_mfma_f32_32x32x16_bf16 v[160:175], v[2:5], v[184:187], v[160:175]
	s_waitcnt lgkmcnt(5)
	v_mfma_f32_32x32x16_bf16 v[144:159], v[8:11], v[184:187], v[144:159]
	s_waitcnt lgkmcnt(4)
	v_mfma_f32_32x32x16_bf16 v[160:175], v[208:211], v[188:191], v[160:175]
	s_waitcnt lgkmcnt(3)
	v_mfma_f32_32x32x16_bf16 v[144:159], v[244:247], v[188:191], v[144:159]
	ds_read_b128 v[244:247], v7 offset:8192
	s_nop 9
	v_exp_f32_e32 v6, v160
	v_exp_f32_e32 v3, v161
	v_exp_f32_e32 v10, v164
	v_exp_f32_e32 v11, v165
	v_exp_f32_e32 v160, v172
	v_exp_f32_e32 v161, v173
	v_exp_f32_e32 v5, v162
	v_exp_f32_e32 v2, v144
	v_exp_f32_e32 v7, v146
	v_exp_f32_e32 v144, v148
	v_exp_f32_e32 v146, v150
	v_exp_f32_e32 v148, v168
	v_exp_f32_e32 v150, v169
	v_exp_f32_e32 v4, v145
	v_exp_f32_e32 v145, v149
	v_exp_f32_e32 v12, v166
	v_exp_f32_e32 v149, v152
	v_exp_f32_e32 v152, v170
	v_exp_f32_e32 v162, v174
	v_exp_f32_e32 v8, v163
	v_exp_f32_e32 v9, v147
	v_exp_f32_e32 v13, v167
	v_exp_f32_e32 v147, v151
	v_exp_f32_e32 v151, v153
	v_exp_f32_e32 v153, v154
	v_exp_f32_e32 v154, v171
	v_exp_f32_e32 v163, v175
	v_exp_f32_e32 v156, v156
	v_exp_f32_e32 v157, v157
	v_add_f32_e32 v164, v6, v3
	v_add_f32_e32 v165, v10, v11
	v_add_f32_e32 v166, v148, v150
	v_add_f32_e32 v167, v160, v161
	v_exp_f32_e32 v158, v158
	v_add_f32_e32 v164, v5, v164
	v_add_f32_e32 v165, v12, v165
	v_add_f32_e32 v166, v152, v166
	v_add_f32_e32 v167, v162, v167
	v_exp_f32_e32 v155, v155
	v_exp_f32_e32 v159, v159
	v_add_f32_e32 v164, v8, v164
	v_add_f32_e32 v165, v13, v165
	v_add_f32_e32 v166, v154, v166
	v_add_f32_e32 v167, v163, v167
	v_add_f32_e32 v164, v2, v164
	v_add_f32_e32 v165, v144, v165
	v_add_f32_e32 v166, v149, v166
	v_add_f32_e32 v167, v156, v167
	v_add_f32_e32 v164, v4, v164
	v_add_f32_e32 v165, v145, v165
	v_add_f32_e32 v166, v151, v166
	v_add_f32_e32 v167, v157, v167
	v_add_f32_e32 v164, v7, v164
	v_add_f32_e32 v165, v146, v165
	v_add_f32_e32 v166, v153, v166
	v_add_f32_e32 v167, v158, v167
	v_add_f32_e32 v164, v9, v164
	v_add_f32_e32 v165, v147, v165
	v_add_f32_e32 v166, v155, v166
	v_add_f32_e32 v167, v159, v167
	v_add_f32_e32 v164, v164, v165
	v_add_f32_e32 v165, v166, v167
	v_add_f32_e32 v213, v164, v165
	v_mov_b32_e32 v218, v213
	v_cvt_pk_bf16_f32 v208, v6, v3
	v_cvt_pk_bf16_f32 v209, v5, v8
	v_cvt_pk_bf16_f32 v210, v10, v11
	v_cvt_pk_bf16_f32 v211, v12, v13
	v_cvt_pk_bf16_f32 v10, v148, v150
	v_cvt_pk_bf16_f32 v11, v152, v154
	v_cvt_pk_bf16_f32 v12, v160, v161
	v_cvt_pk_bf16_f32 v13, v162, v163
	v_cvt_pk_bf16_f32 v6, v2, v4
	v_cvt_pk_bf16_f32 v7, v7, v9
	v_cvt_pk_bf16_f32 v8, v144, v145
	v_cvt_pk_bf16_f32 v9, v146, v147
	v_cvt_pk_bf16_f32 v2, v149, v151
	v_cvt_pk_bf16_f32 v3, v153, v155
	v_cvt_pk_bf16_f32 v4, v156, v157
	v_cvt_pk_bf16_f32 v5, v158, v159
	v_permlane32_swap_b32_e32 v213, v218
	v_permlane32_swap_b32_e32 v208, v210
	v_permlane32_swap_b32_e32 v209, v211
	v_permlane32_swap_b32_e32 v10, v12
	v_permlane32_swap_b32_e32 v11, v13
	v_permlane32_swap_b32_e32 v6, v8
	v_permlane32_swap_b32_e32 v7, v9
	v_permlane32_swap_b32_e32 v2, v4
	v_permlane32_swap_b32_e32 v3, v5
	s_nop 15
	s_nop 15
	s_andn2_b64 vcc, exec, s[44:45]
	s_cbranch_vccnz .Lz_l2s1
	s_andn2_b64 vcc, exec, s[42:43]
	s_mov_b64 s[42:43], -1
	s_cbranch_vccnz .LBB0_218
	v_add_u32_e32 v146, 0x21780, v219
	v_add_u32_e32 v147, 0x21708, v219
	v_add_u32_e32 v148, 0x21788, v219
	ds_read2_b32 v[144:145], v220 offset1:1
	ds_read2_b32 v[160:161], v146 offset1:1
	ds_read2_b32 v[146:147], v147 offset1:1
	ds_read2_b32 v[162:163], v148 offset1:1
	v_add_u32_e32 v148, 0x21720, v219
	v_add_u32_e32 v150, 0x217a0, v219
	v_add_u32_e32 v151, 0x21728, v219
	v_add_u32_e32 v152, 0x217a8, v219
	ds_read2_b32 v[148:149], v148 offset1:1
	ds_read2_b32 v[164:165], v150 offset1:1
	ds_read2_b32 v[150:151], v151 offset1:1
	ds_read2_b32 v[166:167], v152 offset1:1
	v_add_u32_e32 v152, 0x21740, v219
	v_add_u32_e32 v154, 0x217c0, v219
	v_add_u32_e32 v155, 0x21748, v219
	v_add_u32_e32 v156, 0x217c8, v219
	ds_read2_b32 v[152:153], v152 offset1:1
	ds_read2_b32 v[168:169], v154 offset1:1
	ds_read2_b32 v[154:155], v155 offset1:1
	ds_read2_b32 v[170:171], v156 offset1:1
	v_add_u32_e32 v156, 0x21760, v219
	v_add_u32_e32 v158, 0x217e0, v219
	v_add_u32_e32 v159, 0x21768, v219
	v_add_u32_e32 v174, 0x217e8, v219
	ds_read2_b32 v[156:157], v156 offset1:1
	ds_read2_b32 v[172:173], v158 offset1:1
	ds_read2_b32 v[158:159], v159 offset1:1
	ds_read2_b32 v[174:175], v174 offset1:1
	s_mov_b64 s[42:43], 0
